# E17: E15 + slab-quant loop sub-step 4 waits made path-specific (vmcnt 14/12/10/8 when the next-iteration loads were issued) instead of draining the just-issued prefetch
# baseline (speedup 1.0000x reference)
.LBB0_38:
	v_lshl_add_u64 v[2:3], v[86:87], 2, v[2:3]
	s_lshl_b32 s8, s16, 2
	v_lshl_add_u64 v[10:11], v[2:3], 0, s[8:9]
	s_mulk_i32 s16, 0x1fc
	s_mov_b32 s17, s9
	global_load_dwordx4 v[6:9], v[2:3], off nt
	s_nop 0
	global_load_dwordx4 v[2:5], v[10:11], off nt
	v_lshl_add_u64 v[10:11], v[10:11], 0, s[16:17]
	v_lshl_add_u64 v[12:13], v[10:11], 0, s[8:9]
	global_load_dwordx4 v[30:33], v[10:11], off nt
	global_load_dwordx4 v[26:29], v[12:13], off nt
	v_lshl_add_u64 v[10:11], v[12:13], 0, s[16:17]
	v_lshl_add_u64 v[18:19], v[10:11], 0, s[8:9]
	global_load_dwordx4 v[14:17], v[10:11], off nt
	s_nop 0
	global_load_dwordx4 v[10:13], v[18:19], off nt
	v_lshl_add_u64 v[18:19], v[18:19], 0, s[16:17]
	v_lshl_add_u64 v[20:21], v[18:19], 0, s[8:9]
	global_load_dwordx4 v[22:25], v[18:19], off nt
	s_nop 0
	global_load_dwordx4 v[18:21], v[20:21], off nt
	s_waitcnt vmcnt(14)
	v_cvt_pk_bf16_f32 v179, v34, v38
	v_cvt_pk_bf16_f32 v178, v35, v39
	v_cvt_pk_bf16_f32 v177, v36, v40
	v_cvt_pk_bf16_f32 v176, v37, v41
	s_waitcnt vmcnt(12)
	v_cvt_pk_bf16_f32 v174, v42, v46
	v_cvt_pk_bf16_f32 v172, v43, v47
	v_cvt_pk_bf16_f32 v170, v44, v48
	v_cvt_pk_bf16_f32 v168, v45, v49
	s_waitcnt vmcnt(10)
	v_cvt_pk_bf16_f32 v175, v50, v54
	v_cvt_pk_bf16_f32 v173, v51, v55
	v_cvt_pk_bf16_f32 v171, v52, v56
	v_cvt_pk_bf16_f32 v169, v53, v57
	s_waitcnt vmcnt(8)
	v_cvt_pk_bf16_f32 v167, v58, v62
	v_cvt_pk_bf16_f32 v166, v59, v63
	v_cvt_pk_bf16_f32 v165, v60, v64
	v_cvt_pk_bf16_f32 v164, v61, v65
	s_branch .Lslab_join39

.Lslab_join39:
	s_andn2_b64 vcc, exec, s[14:15]
	ds_write2st64_b32 v90, v179, v174 offset0:12 offset1:13
	ds_write2st64_b32 v146, v178, v172 offset0:28 offset1:29
	ds_write2st64_b32 v147, v177, v170 offset0:44 offset1:45
	ds_write2st64_b32 v145, v176, v168 offset0:60 offset1:61
	ds_write2st64_b32 v90, v175, v167 offset0:14 offset1:15
	ds_write2st64_b32 v146, v173, v166 offset0:30 offset1:31
	ds_write2st64_b32 v147, v171, v165 offset0:46 offset1:47
	ds_write2st64_b32 v145, v169, v164 offset0:62 offset1:63
	s_cbranch_vccnz .LBB0_45
	s_cmpk_gt_i32 s45, 0x17ff
	s_mov_b64 s[16:17], -1
	s_cbranch_scc0 .LBB0_42
	v_add_u32_e32 v0, s44, v103
	v_cmp_gt_u32_e32 vcc, s37, v0
	s_mov_b64 s[16:17], 0
	s_nop 0
	v_cndmask_b32_e32 v86, 0, v0, vcc

.LBB0_97:
	s_waitcnt lgkmcnt(0)
	v_cmp_lt_i32_e32 vcc, -1, v86
	s_and_saveexec_b64 s[10:11], vcc
	s_cbranch_execz .LBB0_24
	ds_read2_b64 v[116:119], v106 offset1:1
	ds_read2_b64 v[120:123], v106 offset0:2 offset1:3
	v_lshlrev_b64 v[88:89], 11, v[86:87]
	v_readlane_b32 s14, v252, 2
	v_readlane_b32 s15, v252, 3
	s_waitcnt lgkmcnt(1)
	v_lshlrev_b32_e32 v0, 16, v116
	v_and_b32_e32 v86, 0xffff0000, v116
	v_lshlrev_b32_e32 v116, 16, v117
	v_and_b32_e32 v117, 0xffff0000, v117
	v_fmaak_f32 v0, v115, v0, 0x4b400000
	v_fmaak_f32 v86, v115, v86, 0x4b400000
	v_fmaak_f32 v116, v115, v116, 0x4b400000
	v_fmaak_f32 v117, v115, v117, 0x4b400000
	v_perm_b32 v0, v86, v0, s43
	v_perm_b32 v86, v117, v116, s43
	v_lshl_or_b32 v116, v86, 16, v0
	v_lshlrev_b32_e32 v0, 16, v118
	v_and_b32_e32 v86, 0xffff0000, v118
	v_lshlrev_b32_e32 v117, 16, v119
	v_and_b32_e32 v118, 0xffff0000, v119
	v_fmaak_f32 v0, v115, v0, 0x4b400000
	v_fmaak_f32 v86, v115, v86, 0x4b400000
	v_fmaak_f32 v117, v115, v117, 0x4b400000
	v_fmaak_f32 v118, v115, v118, 0x4b400000
	v_perm_b32 v0, v86, v0, s43
	v_perm_b32 v86, v118, v117, s43
	v_lshl_or_b32 v117, v86, 16, v0
	s_waitcnt lgkmcnt(0)
	v_lshlrev_b32_e32 v0, 16, v120
	v_and_b32_e32 v86, 0xffff0000, v120
	v_lshlrev_b32_e32 v118, 16, v121
	v_and_b32_e32 v119, 0xffff0000, v121
	v_fmaak_f32 v0, v115, v0, 0x4b400000
	v_fmaak_f32 v86, v115, v86, 0x4b400000
	v_fmaak_f32 v118, v115, v118, 0x4b400000
	v_fmaak_f32 v119, v115, v119, 0x4b400000
	v_perm_b32 v0, v86, v0, s43
	v_perm_b32 v86, v119, v118, s43
	v_lshl_or_b32 v118, v86, 16, v0
	v_lshlrev_b32_e32 v0, 16, v122
	v_and_b32_e32 v86, 0xffff0000, v122
	v_lshlrev_b32_e32 v119, 16, v123
	v_and_b32_e32 v120, 0xffff0000, v123
	v_fmaak_f32 v0, v115, v0, 0x4b400000
	v_fmaak_f32 v86, v115, v86, 0x4b400000
	v_fmaak_f32 v119, v115, v119, 0x4b400000
	v_fmaak_f32 v120, v115, v120, 0x4b400000
	v_perm_b32 v0, v86, v0, s43
	v_perm_b32 v86, v120, v119, s43
	ds_read2_b64 v[120:123], v107 offset1:1
	s_add_u32 s12, s14, s12
	s_addc_u32 s13, s15, s13
	v_lshl_add_u64 v[88:89], s[12:13], 0, v[88:89]
	v_lshl_or_b32 v119, v86, 16, v0
	v_lshl_add_u64 v[124:125], v[88:89], 0, v[68:69]
	global_store_dwordx4 v[124:125], v[116:119], off nt
	ds_read2_b64 v[116:119], v107 offset0:2 offset1:3
	s_waitcnt lgkmcnt(1)
	v_lshlrev_b32_e32 v0, 16, v120
	v_and_b32_e32 v86, 0xffff0000, v120
	v_lshlrev_b32_e32 v120, 16, v121
	v_and_b32_e32 v121, 0xffff0000, v121
	v_fmaak_f32 v0, v115, v0, 0x4b400000
	v_fmaak_f32 v86, v115, v86, 0x4b400000
	v_fmaak_f32 v120, v115, v120, 0x4b400000
	v_fmaak_f32 v121, v115, v121, 0x4b400000
	v_perm_b32 v0, v86, v0, s43
	v_perm_b32 v86, v121, v120, s43
	v_lshl_or_b32 v120, v86, 16, v0
	v_lshlrev_b32_e32 v0, 16, v122
	v_and_b32_e32 v86, 0xffff0000, v122
	v_lshlrev_b32_e32 v121, 16, v123
	v_and_b32_e32 v122, 0xffff0000, v123
	v_fmaak_f32 v0, v115, v0, 0x4b400000
	v_fmaak_f32 v86, v115, v86, 0x4b400000
	v_fmaak_f32 v121, v115, v121, 0x4b400000
	v_fmaak_f32 v122, v115, v122, 0x4b400000
	v_perm_b32 v0, v86, v0, s43
	v_perm_b32 v86, v122, v121, s43
	v_lshl_or_b32 v121, v86, 16, v0
	s_waitcnt lgkmcnt(0)
	v_lshlrev_b32_e32 v0, 16, v116
	v_and_b32_e32 v86, 0xffff0000, v116
	v_lshlrev_b32_e32 v116, 16, v117
	v_and_b32_e32 v117, 0xffff0000, v117
	v_fmaak_f32 v0, v115, v0, 0x4b400000
	v_fmaak_f32 v86, v115, v86, 0x4b400000
	v_fmaak_f32 v116, v115, v116, 0x4b400000
	v_fmaak_f32 v117, v115, v117, 0x4b400000
	v_perm_b32 v0, v86, v0, s43
	v_perm_b32 v86, v117, v116, s43
	v_lshl_or_b32 v122, v86, 16, v0
	v_lshlrev_b32_e32 v0, 16, v118
	v_and_b32_e32 v86, 0xffff0000, v118
	v_lshlrev_b32_e32 v116, 16, v119
	v_and_b32_e32 v117, 0xffff0000, v119
	v_fmaak_f32 v0, v115, v0, 0x4b400000
	v_fmaak_f32 v86, v115, v86, 0x4b400000
	v_fmaak_f32 v116, v115, v116, 0x4b400000
	v_fmaak_f32 v117, v115, v117, 0x4b400000
	v_perm_b32 v0, v86, v0, s43
	v_perm_b32 v86, v117, v116, s43
	ds_read2_b64 v[116:119], v108 offset1:1
	v_lshl_or_b32 v123, v86, 16, v0
	v_lshl_add_u64 v[124:125], v[88:89], 0, v[70:71]
	global_store_dwordx4 v[124:125], v[120:123], off nt
	ds_read2_b64 v[120:123], v108 offset0:2 offset1:3
	s_waitcnt lgkmcnt(1)
	v_lshlrev_b32_e32 v0, 16, v116
	v_and_b32_e32 v86, 0xffff0000, v116
	v_lshlrev_b32_e32 v116, 16, v117
	v_and_b32_e32 v117, 0xffff0000, v117
	v_fmaak_f32 v0, v115, v0, 0x4b400000
	v_fmaak_f32 v86, v115, v86, 0x4b400000
	v_fmaak_f32 v116, v115, v116, 0x4b400000
	v_fmaak_f32 v117, v115, v117, 0x4b400000
	v_perm_b32 v0, v86, v0, s43
	v_perm_b32 v86, v117, v116, s43
	v_lshl_or_b32 v116, v86, 16, v0
	v_lshlrev_b32_e32 v0, 16, v118
	v_and_b32_e32 v86, 0xffff0000, v118
	v_lshlrev_b32_e32 v117, 16, v119
	v_and_b32_e32 v118, 0xffff0000, v119
	v_fmaak_f32 v0, v115, v0, 0x4b400000
	v_fmaak_f32 v86, v115, v86, 0x4b400000
	v_fmaak_f32 v117, v115, v117, 0x4b400000
	v_fmaak_f32 v118, v115, v118, 0x4b400000
	v_perm_b32 v0, v86, v0, s43
	v_perm_b32 v86, v118, v117, s43
	v_lshl_or_b32 v117, v86, 16, v0
	s_waitcnt lgkmcnt(0)
	v_lshlrev_b32_e32 v0, 16, v120
	v_and_b32_e32 v86, 0xffff0000, v120
	v_lshlrev_b32_e32 v118, 16, v121
	v_and_b32_e32 v119, 0xffff0000, v121
	v_fmaak_f32 v0, v115, v0, 0x4b400000
	v_fmaak_f32 v86, v115, v86, 0x4b400000
	v_fmaak_f32 v118, v115, v118, 0x4b400000
	v_fmaak_f32 v119, v115, v119, 0x4b400000
	v_perm_b32 v0, v86, v0, s43
	v_perm_b32 v86, v119, v118, s43
	v_lshl_or_b32 v118, v86, 16, v0
	v_lshlrev_b32_e32 v0, 16, v122
	v_and_b32_e32 v86, 0xffff0000, v122
	v_lshlrev_b32_e32 v119, 16, v123
	v_and_b32_e32 v120, 0xffff0000, v123
	v_fmaak_f32 v0, v115, v0, 0x4b400000
	v_fmaak_f32 v86, v115, v86, 0x4b400000
	v_fmaak_f32 v119, v115, v119, 0x4b400000
	v_fmaak_f32 v120, v115, v120, 0x4b400000
	v_perm_b32 v0, v86, v0, s43
	v_perm_b32 v86, v120, v119, s43
	ds_read2_b64 v[120:123], v109 offset1:1
	v_lshl_or_b32 v119, v86, 16, v0
	v_lshl_add_u64 v[124:125], v[88:89], 0, v[72:73]
	global_store_dwordx4 v[124:125], v[116:119], off nt
	ds_read2_b64 v[116:119], v109 offset0:2 offset1:3
	s_waitcnt lgkmcnt(1)
	v_lshlrev_b32_e32 v0, 16, v120
	v_and_b32_e32 v86, 0xffff0000, v120
	v_lshlrev_b32_e32 v120, 16, v121
	v_and_b32_e32 v121, 0xffff0000, v121
	v_fmaak_f32 v0, v115, v0, 0x4b400000
	v_fmaak_f32 v86, v115, v86, 0x4b400000
	v_fmaak_f32 v120, v115, v120, 0x4b400000
	v_fmaak_f32 v121, v115, v121, 0x4b400000
	v_perm_b32 v0, v86, v0, s43
	v_perm_b32 v86, v121, v120, s43
	v_lshl_or_b32 v120, v86, 16, v0
	v_lshlrev_b32_e32 v0, 16, v122
	v_and_b32_e32 v86, 0xffff0000, v122
	v_lshlrev_b32_e32 v121, 16, v123
	v_and_b32_e32 v122, 0xffff0000, v123
	v_fmaak_f32 v0, v115, v0, 0x4b400000
	v_fmaak_f32 v86, v115, v86, 0x4b400000
	v_fmaak_f32 v121, v115, v121, 0x4b400000
	v_fmaak_f32 v122, v115, v122, 0x4b400000
	v_perm_b32 v0, v86, v0, s43
	v_perm_b32 v86, v122, v121, s43
	v_lshl_or_b32 v121, v86, 16, v0
	s_waitcnt lgkmcnt(0)
	v_lshlrev_b32_e32 v0, 16, v116
	v_and_b32_e32 v86, 0xffff0000, v116
	v_lshlrev_b32_e32 v116, 16, v117
	v_and_b32_e32 v117, 0xffff0000, v117
	v_fmaak_f32 v0, v115, v0, 0x4b400000
	v_fmaak_f32 v86, v115, v86, 0x4b400000
	v_fmaak_f32 v116, v115, v116, 0x4b400000
	v_fmaak_f32 v117, v115, v117, 0x4b400000
	v_perm_b32 v0, v86, v0, s43
	v_perm_b32 v86, v117, v116, s43
	v_lshl_or_b32 v122, v86, 16, v0
	v_lshlrev_b32_e32 v0, 16, v118
	v_and_b32_e32 v86, 0xffff0000, v118
	v_lshlrev_b32_e32 v116, 16, v119
	v_and_b32_e32 v117, 0xffff0000, v119
	v_fmaak_f32 v0, v115, v0, 0x4b400000
	v_fmaak_f32 v86, v115, v86, 0x4b400000
	v_fmaak_f32 v116, v115, v116, 0x4b400000
	v_fmaak_f32 v117, v115, v117, 0x4b400000
	v_perm_b32 v0, v86, v0, s43
	v_perm_b32 v86, v117, v116, s43
	ds_read2_b64 v[116:119], v110 offset1:1
	v_lshl_or_b32 v123, v86, 16, v0
	v_lshl_add_u64 v[124:125], v[88:89], 0, v[74:75]
	global_store_dwordx4 v[124:125], v[120:123], off nt
	ds_read2_b64 v[120:123], v110 offset0:2 offset1:3
	s_waitcnt lgkmcnt(1)
	v_lshlrev_b32_e32 v0, 16, v116
	v_and_b32_e32 v86, 0xffff0000, v116
	v_lshlrev_b32_e32 v116, 16, v117
	v_and_b32_e32 v117, 0xffff0000, v117
	v_fmaak_f32 v0, v115, v0, 0x4b400000
	v_fmaak_f32 v86, v115, v86, 0x4b400000
	v_fmaak_f32 v116, v115, v116, 0x4b400000
	v_fmaak_f32 v117, v115, v117, 0x4b400000
	v_perm_b32 v0, v86, v0, s43
	v_perm_b32 v86, v117, v116, s43
	v_lshl_or_b32 v116, v86, 16, v0
	v_lshlrev_b32_e32 v0, 16, v118
	v_and_b32_e32 v86, 0xffff0000, v118
	v_lshlrev_b32_e32 v117, 16, v119
	v_and_b32_e32 v118, 0xffff0000, v119
	v_fmaak_f32 v0, v115, v0, 0x4b400000
	v_fmaak_f32 v86, v115, v86, 0x4b400000
	v_fmaak_f32 v117, v115, v117, 0x4b400000
	v_fmaak_f32 v118, v115, v118, 0x4b400000
	v_perm_b32 v0, v86, v0, s43
	v_perm_b32 v86, v118, v117, s43
	v_lshl_or_b32 v117, v86, 16, v0
	s_waitcnt lgkmcnt(0)
	v_lshlrev_b32_e32 v0, 16, v120
	v_and_b32_e32 v86, 0xffff0000, v120
	v_lshlrev_b32_e32 v118, 16, v121
	v_and_b32_e32 v119, 0xffff0000, v121
	v_fmaak_f32 v0, v115, v0, 0x4b400000
	v_fmaak_f32 v86, v115, v86, 0x4b400000
	v_fmaak_f32 v118, v115, v118, 0x4b400000
	v_fmaak_f32 v119, v115, v119, 0x4b400000
	v_perm_b32 v0, v86, v0, s43
	v_perm_b32 v86, v119, v118, s43
	v_lshl_or_b32 v118, v86, 16, v0
	v_lshlrev_b32_e32 v0, 16, v122
	v_and_b32_e32 v86, 0xffff0000, v122
	v_lshlrev_b32_e32 v119, 16, v123
	v_and_b32_e32 v120, 0xffff0000, v123
	v_fmaak_f32 v0, v115, v0, 0x4b400000
	v_fmaak_f32 v86, v115, v86, 0x4b400000
	v_fmaak_f32 v119, v115, v119, 0x4b400000
	v_fmaak_f32 v120, v115, v120, 0x4b400000
	v_perm_b32 v0, v86, v0, s43
	v_perm_b32 v86, v120, v119, s43
	ds_read2_b64 v[120:123], v111 offset1:1
	v_lshl_or_b32 v119, v86, 16, v0
	v_lshl_add_u64 v[124:125], v[88:89], 0, v[76:77]
	global_store_dwordx4 v[124:125], v[116:119], off nt
	ds_read2_b64 v[116:119], v111 offset0:2 offset1:3
	s_waitcnt lgkmcnt(1)
	v_lshlrev_b32_e32 v0, 16, v120
	v_and_b32_e32 v86, 0xffff0000, v120
	v_lshlrev_b32_e32 v120, 16, v121
	v_and_b32_e32 v121, 0xffff0000, v121
	v_fmaak_f32 v0, v115, v0, 0x4b400000
	v_fmaak_f32 v86, v115, v86, 0x4b400000
	v_fmaak_f32 v120, v115, v120, 0x4b400000
	v_fmaak_f32 v121, v115, v121, 0x4b400000
	v_perm_b32 v0, v86, v0, s43
	v_perm_b32 v86, v121, v120, s43
	v_lshl_or_b32 v120, v86, 16, v0
	v_lshlrev_b32_e32 v0, 16, v122
	v_and_b32_e32 v86, 0xffff0000, v122
	v_lshlrev_b32_e32 v121, 16, v123
	v_and_b32_e32 v122, 0xffff0000, v123
	v_fmaak_f32 v0, v115, v0, 0x4b400000
	v_fmaak_f32 v86, v115, v86, 0x4b400000
	v_fmaak_f32 v121, v115, v121, 0x4b400000
	v_fmaak_f32 v122, v115, v122, 0x4b400000
	v_perm_b32 v0, v86, v0, s43
	v_perm_b32 v86, v122, v121, s43
	v_lshl_or_b32 v121, v86, 16, v0
	s_waitcnt lgkmcnt(0)
	v_lshlrev_b32_e32 v0, 16, v116
	v_and_b32_e32 v86, 0xffff0000, v116
	v_lshlrev_b32_e32 v116, 16, v117
	v_and_b32_e32 v117, 0xffff0000, v117
	v_fmaak_f32 v0, v115, v0, 0x4b400000
	v_fmaak_f32 v86, v115, v86, 0x4b400000
	v_fmaak_f32 v116, v115, v116, 0x4b400000
	v_fmaak_f32 v117, v115, v117, 0x4b400000
	v_perm_b32 v0, v86, v0, s43
	v_perm_b32 v86, v117, v116, s43
	v_lshl_or_b32 v122, v86, 16, v0
	v_lshlrev_b32_e32 v0, 16, v118
	v_and_b32_e32 v86, 0xffff0000, v118
	v_lshlrev_b32_e32 v116, 16, v119
	v_and_b32_e32 v117, 0xffff0000, v119
	v_fmaak_f32 v0, v115, v0, 0x4b400000
	v_fmaak_f32 v86, v115, v86, 0x4b400000
	v_fmaak_f32 v116, v115, v116, 0x4b400000
	v_fmaak_f32 v117, v115, v117, 0x4b400000
	v_perm_b32 v0, v86, v0, s43
	v_perm_b32 v86, v117, v116, s43
	ds_read2_b64 v[116:119], v112 offset1:1
	v_lshl_or_b32 v123, v86, 16, v0
	v_lshl_add_u64 v[124:125], v[88:89], 0, v[78:79]
	global_store_dwordx4 v[124:125], v[120:123], off nt
	ds_read2_b64 v[120:123], v112 offset0:2 offset1:3
	s_waitcnt lgkmcnt(1)
	v_lshlrev_b32_e32 v0, 16, v116
	v_and_b32_e32 v86, 0xffff0000, v116
	v_lshlrev_b32_e32 v116, 16, v117
	v_and_b32_e32 v117, 0xffff0000, v117
	v_fmaak_f32 v0, v115, v0, 0x4b400000
	v_fmaak_f32 v86, v115, v86, 0x4b400000
	v_fmaak_f32 v116, v115, v116, 0x4b400000
	v_fmaak_f32 v117, v115, v117, 0x4b400000
	v_perm_b32 v0, v86, v0, s43
	v_perm_b32 v86, v117, v116, s43
	v_lshl_or_b32 v116, v86, 16, v0
	v_lshlrev_b32_e32 v0, 16, v118
	v_and_b32_e32 v86, 0xffff0000, v118
	v_lshlrev_b32_e32 v117, 16, v119
	v_and_b32_e32 v118, 0xffff0000, v119
	v_fmaak_f32 v0, v115, v0, 0x4b400000
	v_fmaak_f32 v86, v115, v86, 0x4b400000
	v_fmaak_f32 v117, v115, v117, 0x4b400000
	v_fmaak_f32 v118, v115, v118, 0x4b400000
	v_perm_b32 v0, v86, v0, s43
	v_perm_b32 v86, v118, v117, s43
	v_lshl_or_b32 v117, v86, 16, v0
	s_waitcnt lgkmcnt(0)
	v_lshlrev_b32_e32 v0, 16, v120
	v_and_b32_e32 v86, 0xffff0000, v120
	v_lshlrev_b32_e32 v118, 16, v121
	v_and_b32_e32 v119, 0xffff0000, v121
	v_fmaak_f32 v0, v115, v0, 0x4b400000
	v_fmaak_f32 v86, v115, v86, 0x4b400000
	v_fmaak_f32 v118, v115, v118, 0x4b400000
	v_fmaak_f32 v119, v115, v119, 0x4b400000
	v_perm_b32 v0, v86, v0, s43
	v_perm_b32 v86, v119, v118, s43
	v_lshl_or_b32 v118, v86, 16, v0
	v_lshlrev_b32_e32 v0, 16, v122
	v_and_b32_e32 v86, 0xffff0000, v122
	v_lshlrev_b32_e32 v119, 16, v123
	v_and_b32_e32 v120, 0xffff0000, v123
	v_fmaak_f32 v0, v115, v0, 0x4b400000
	v_fmaak_f32 v86, v115, v86, 0x4b400000
	v_fmaak_f32 v119, v115, v119, 0x4b400000
	v_fmaak_f32 v120, v115, v120, 0x4b400000
	v_perm_b32 v0, v86, v0, s43
	v_perm_b32 v86, v120, v119, s43
	ds_read2_b64 v[120:123], v113 offset1:1
	v_lshl_or_b32 v119, v86, 16, v0
	v_lshl_add_u64 v[124:125], v[88:89], 0, v[80:81]
	global_store_dwordx4 v[124:125], v[116:119], off nt
	ds_read2_b64 v[116:119], v113 offset0:2 offset1:3
	s_waitcnt lgkmcnt(1)
	v_lshlrev_b32_e32 v0, 16, v120
	v_and_b32_e32 v86, 0xffff0000, v120
	v_lshlrev_b32_e32 v120, 16, v121
	v_and_b32_e32 v121, 0xffff0000, v121
	v_fmaak_f32 v0, v115, v0, 0x4b400000
	v_fmaak_f32 v86, v115, v86, 0x4b400000
	v_fmaak_f32 v120, v115, v120, 0x4b400000
	v_fmaak_f32 v121, v115, v121, 0x4b400000
	v_perm_b32 v0, v86, v0, s43
	v_perm_b32 v86, v121, v120, s43
	v_lshl_or_b32 v120, v86, 16, v0
	v_lshlrev_b32_e32 v0, 16, v122
	v_and_b32_e32 v86, 0xffff0000, v122
	v_lshlrev_b32_e32 v121, 16, v123
	v_and_b32_e32 v122, 0xffff0000, v123
	v_fmaak_f32 v0, v115, v0, 0x4b400000
	v_fmaak_f32 v86, v115, v86, 0x4b400000
	v_fmaak_f32 v121, v115, v121, 0x4b400000
	v_fmaak_f32 v122, v115, v122, 0x4b400000
	v_perm_b32 v0, v86, v0, s43
	v_perm_b32 v86, v122, v121, s43
	v_lshl_or_b32 v121, v86, 16, v0
	s_waitcnt lgkmcnt(0)
	v_lshlrev_b32_e32 v0, 16, v116
	v_and_b32_e32 v86, 0xffff0000, v116
	v_lshlrev_b32_e32 v116, 16, v117
	v_and_b32_e32 v117, 0xffff0000, v117
	v_fmaak_f32 v0, v115, v0, 0x4b400000
	v_fmaak_f32 v86, v115, v86, 0x4b400000
	v_fmaak_f32 v116, v115, v116, 0x4b400000
	v_fmaak_f32 v117, v115, v117, 0x4b400000
	v_perm_b32 v0, v86, v0, s43
	v_perm_b32 v86, v117, v116, s43
	v_lshl_or_b32 v122, v86, 16, v0
	v_lshlrev_b32_e32 v0, 16, v118
	v_and_b32_e32 v86, 0xffff0000, v118
	v_lshlrev_b32_e32 v116, 16, v119
	v_and_b32_e32 v117, 0xffff0000, v119
	v_fmaak_f32 v0, v115, v0, 0x4b400000
	v_fmaak_f32 v86, v115, v86, 0x4b400000
	v_fmaak_f32 v116, v115, v116, 0x4b400000
	v_fmaak_f32 v115, v115, v117, 0x4b400000
	v_perm_b32 v0, v86, v0, s43
	v_perm_b32 v86, v115, v116, s43
	v_lshl_or_b32 v123, v86, 16, v0
	v_lshl_add_u64 v[88:89], v[88:89], 0, v[82:83]
	global_store_dwordx4 v[88:89], v[120:123], off nt
	s_branch .LBB0_24
	s_nop 0
	s_nop 0
	s_nop 0
	s_nop 0
	s_nop 0
	s_nop 0
	s_nop 0
	s_nop 0
	s_nop 0
	s_nop 0
	s_nop 0
